# stream block behind the last PV MFMA (counted wait for the K/V pieces at the step end as in the baseline)
# speedup vs baseline: 1.0111x; 1.0004x over previous
; #define LAS __attribute__((address_space(3)))
; __device__ __forceinline__ unsigned pk2(float lo, float hi) { return f2bf(lo) | (f2bf(hi) << 16); }
;     __device__ __forceinline__ const float* x() const { return (const float*)ld(0); }
;     __device__ __forceinline__ const float* c() const { return (const float*)ld(1); }
; template <bool NT = true> __device__ __forceinline__ void cvt_store(const CvtItem& d, const f32x4 (&v)[8], LAS float* scr, int lane) {
;     const int rr = lane >> 3, c4 = (lane & 7) * 4;
; #pragma unroll
;     for (int q = 0; q < 8; ++q) { LAS float* t = scr + (8 * q + rr) * 33 + c4; t[0] = v[q].x; t[1] = v[q].y; t[2] = v[q].z; t[3] = v[q].w; }
;     asm volatile("s_waitcnt lgkmcnt(0)" ::: "memory");
;     const int c = lane & 7;
; #pragma unroll
;     for (int j = 0; j < 4; ++j) { const int n = (lane >> 3) + 8 * j; const LAS float* s = scr + (8 * c) * 33 + n;
;         u32x4 o; o.x = pk2(s[0 * 33], s[1 * 33]); o.y = pk2(s[2 * 33], s[3 * 33]); o.z = pk2(s[4 * 33], s[5 * 33]); o.w = pk2(s[6 * 33], s[7 * 33]);
;         const int ng = d.n0 + n, drow = d.row_off + (d.ilv ? ((ng >> 7) * 256 + (ng & 127)) : ng);
;         if (NT) __builtin_nontemporal_store(o, (u32x4*)(d.dst + (size_t)drow * d.K + d.k0 + 8 * c)); else *(u32x4*)(d.dst + (size_t)drow * d.K + d.k0 + 8 * c) = o; }
;     asm volatile("s_waitcnt lgkmcnt(0)" ::: "memory");
.LBB0_529:
	v_mfma_f32_32x32x16_bf16 v[66:81], v[194:197], v[134:137], v[66:81]
	v_exp_f32_e32 v162, v162
	v_exp_f32_e32 v163, v163
	ds_read_b64_tr_b16 v[122:123], v16 offset:50176
	ds_read_b64_tr_b16 v[124:125], v16 offset:50688
	s_add_u32 s58, s33, 0xfef80000
	s_addc_u32 s59, s53, -1
	s_add_u32 s2, s33, 0xfefe0000
	s_addc_u32 s3, s53, -1
	s_add_i32 s60, s57, s49
	s_mov_b32 s61, m0
	s_mov_b32 m0, s60
	s_nop 0
	global_load_lds_dwordx4 v237, s[2:3] offset:0
	s_mov_b32 m0, s61
	v_mfma_f32_32x32x16_bf16 v[82:97], v[194:197], v[130:133], v[82:97]
	v_exp_f32_e32 v164, v164
	v_exp_f32_e32 v165, v165
	ds_read_b64_tr_b16 v[126:127], v16 offset:54272
	ds_read_b64_tr_b16 v[128:129], v16 offset:54784
	s_waitcnt lgkmcnt(6)
	v_mfma_f32_32x32x16_bf16 v[34:49], v[194:197], v[118:121], v[34:49]
	v_exp_f32_e32 v166, v166
	v_exp_f32_e32 v167, v167
	ds_read_b64_tr_b16 v[130:131], v16 offset:58368
	ds_read_b64_tr_b16 v[132:133], v16 offset:58880
	s_add_u32 s2, s33, 0xfefe0080
	s_addc_u32 s3, s53, -1
	s_add_i32 s60, s57, s54
	s_mov_b32 s61, m0
	s_mov_b32 m0, s60
	s_nop 0
	global_load_lds_dwordx4 v237, s[2:3] offset:0
	s_mov_b32 m0, s61
	s_waitcnt lgkmcnt(6)
	v_mfma_f32_32x32x16_bf16 v[50:65], v[194:197], v[114:117], v[50:65]
	v_exp_f32_e32 v168, v168
	v_exp_f32_e32 v169, v169
	ds_read_b64_tr_b16 v[118:119], v16 offset:62464
	ds_read_b64_tr_b16 v[120:121], v16 offset:62976
	v_add_u32_e32 v17, s55, v236
	ds_read_b128 v[114:117], v17
	ds_read_b128 v[178:181], v17 offset:512
	s_waitcnt lgkmcnt(8)
	v_mfma_f32_32x32x16_bf16 v[66:81], v[12:15], v[122:125], v[66:81]
	v_exp_f32_e32 v170, v170
	v_exp_f32_e32 v171, v171
	ds_read_b64_tr_b16 v[134:135], v16 offset:51200
	ds_read_b64_tr_b16 v[136:137], v16 offset:51712
	s_add_u32 s2, s33, 0x20000
	s_addc_u32 s3, s53, 0
	s_add_i32 s60, s55, s46
	s_mov_b32 s61, m0
	s_mov_b32 m0, s60
	s_nop 0
	global_load_lds_dwordx4 v235, s[2:3] offset:0
	s_mov_b32 m0, s61
	s_waitcnt lgkmcnt(8)
	v_mfma_f32_32x32x16_bf16 v[82:97], v[12:15], v[126:129], v[82:97]
	v_exp_f32_e32 v172, v172
	v_exp_f32_e32 v173, v173
	ds_read_b64_tr_b16 v[122:123], v16 offset:55296
	ds_read_b64_tr_b16 v[124:125], v16 offset:55808
	ds_read_b128 v[198:201], v17 offset:2048
	ds_read_b128 v[186:189], v17 offset:2560
	s_waitcnt lgkmcnt(10)
	v_mfma_f32_32x32x16_bf16 v[34:49], v[12:15], v[130:133], v[34:49]
	v_exp_f32_e32 v174, v174
	v_exp_f32_e32 v175, v175
	ds_read_b64_tr_b16 v[126:127], v16 offset:59392
	ds_read_b64_tr_b16 v[128:129], v16 offset:59904
	s_add_u32 s2, s33, 0x20080
	s_addc_u32 s3, s53, 0
	s_add_i32 s60, s55, s45
	s_mov_b32 s61, m0
	s_mov_b32 m0, s60
	s_nop 0
	global_load_lds_dwordx4 v235, s[2:3] offset:0
	s_mov_b32 m0, s61
	s_waitcnt lgkmcnt(10)
	v_mfma_f32_32x32x16_bf16 v[50:65], v[12:15], v[118:121], v[50:65]
	v_exp_f32_e32 v176, v176
	v_exp_f32_e32 v177, v177
	ds_read_b64_tr_b16 v[130:131], v16 offset:63488
	ds_read_b64_tr_b16 v[132:133], v16 offset:64000
	ds_read_b128 v[206:209], v17 offset:4096
	ds_read_b128 v[190:193], v17 offset:4608
	s_waitcnt lgkmcnt(10)
	v_mfma_f32_32x32x16_bf16 v[66:81], v[8:11], v[134:137], v[66:81]
	v_exp_f32_e32 v146, v146
	v_exp_f32_e32 v147, v147
	ds_read_b64_tr_b16 v[118:119], v16 offset:52224
	ds_read_b64_tr_b16 v[120:121], v16 offset:52736
	s_waitcnt lgkmcnt(10)
	v_mfma_f32_32x32x16_bf16 v[82:97], v[8:11], v[122:125], v[82:97]
	v_exp_f32_e32 v148, v148
	v_exp_f32_e32 v149, v149
	ds_read_b64_tr_b16 v[134:135], v16 offset:56320
	ds_read_b64_tr_b16 v[136:137], v16 offset:56832
	ds_read_b128 v[202:205], v17 offset:6144
	ds_read_b128 v[182:185], v17 offset:6656
	s_waitcnt lgkmcnt(10)
	v_mfma_f32_32x32x16_bf16 v[34:49], v[8:11], v[126:129], v[34:49]
	v_exp_f32_e32 v150, v150
	v_exp_f32_e32 v151, v151
	ds_read_b64_tr_b16 v[122:123], v16 offset:60416
	ds_read_b64_tr_b16 v[124:125], v16 offset:60928
	s_waitcnt lgkmcnt(10)
	v_mfma_f32_32x32x16_bf16 v[50:65], v[8:11], v[130:133], v[50:65]
	v_exp_f32_e32 v152, v152
	v_exp_f32_e32 v153, v153
	ds_read_b64_tr_b16 v[126:127], v16 offset:64512
	ds_read_b64_tr_b16 v[128:129], v16 offset:65024
	s_waitcnt lgkmcnt(8)
	v_mfma_f32_32x32x16_bf16 v[66:81], v[4:7], v[118:121], v[66:81]
	v_exp_f32_e32 v154, v154
	v_exp_f32_e32 v155, v155
	s_waitcnt lgkmcnt(6)
	v_mfma_f32_32x32x16_bf16 v[82:97], v[4:7], v[134:137], v[82:97]
	v_exp_f32_e32 v156, v156
	v_exp_f32_e32 v157, v157
	s_waitcnt lgkmcnt(2)
	v_mfma_f32_32x32x16_bf16 v[34:49], v[4:7], v[122:125], v[34:49]
	v_exp_f32_e32 v158, v158
	v_exp_f32_e32 v159, v159
	s_waitcnt lgkmcnt(0)
	v_mfma_f32_32x32x16_bf16 v[50:65], v[4:7], v[126:129], v[50:65]
	v_exp_f32_e32 v160, v160
	v_exp_f32_e32 v161, v161
	s_add_i32 s2, s56, 1
	s_cmp_gt_i32 s2, s90
	s_cbranch_scc1 .Lcs_done_h0
	s_waitcnt vmcnt(6)
	v_cvt_pk_bf16_f32 v245, v250, v251
	v_cvt_pk_bf16_f32 v244, v252, v253
	s_cmp_lt_u32 s2, 7
	s_cbranch_scc1 .Lcs_dumS_h0
	s_bitcmp1_b32 s2, 1
	s_cbranch_scc1 .Lcs_Sb_h0
	global_store_dwordx2 v28, v[30:31], s[100:101] nt
	v_add_u32_e32 v28, s63, v28

; #define LAS __attribute__((address_space(3)))
; __device__ __forceinline__ unsigned pk2(float lo, float hi) { return f2bf(lo) | (f2bf(hi) << 16); }
;     __device__ __forceinline__ const float* x() const { return (const float*)ld(0); }
;     __device__ __forceinline__ const float* c() const { return (const float*)ld(1); }
; template <bool NT = true> __device__ __forceinline__ void cvt_store(const CvtItem& d, const f32x4 (&v)[8], LAS float* scr, int lane) {
;     const int rr = lane >> 3, c4 = (lane & 7) * 4;
; #pragma unroll
;     for (int q = 0; q < 8; ++q) { LAS float* t = scr + (8 * q + rr) * 33 + c4; t[0] = v[q].x; t[1] = v[q].y; t[2] = v[q].z; t[3] = v[q].w; }
;     asm volatile("s_waitcnt lgkmcnt(0)" ::: "memory");
;     const int c = lane & 7;
; #pragma unroll
;     for (int j = 0; j < 4; ++j) { const int n = (lane >> 3) + 8 * j; const LAS float* s = scr + (8 * c) * 33 + n;
;         u32x4 o; o.x = pk2(s[0 * 33], s[1 * 33]); o.y = pk2(s[2 * 33], s[3 * 33]); o.z = pk2(s[4 * 33], s[5 * 33]); o.w = pk2(s[6 * 33], s[7 * 33]);
;         const int ng = d.n0 + n, drow = d.row_off + (d.ilv ? ((ng >> 7) * 256 + (ng & 127)) : ng);
;         if (NT) __builtin_nontemporal_store(o, (u32x4*)(d.dst + (size_t)drow * d.K + d.k0 + 8 * c)); else *(u32x4*)(d.dst + (size_t)drow * d.K + d.k0 + 8 * c) = o; }
;     asm volatile("s_waitcnt lgkmcnt(0)" ::: "memory");
.Lcs_noL_h0:
	s_waitcnt lgkmcnt(0)
	s_cmp_gt_i32 s2, s90
	s_cbranch_scc1 .Lcs_noW_h0
	s_bitcmp1_b32 s2, 1
	s_cbranch_scc1 .Lcs_R_h0

; #define LAS __attribute__((address_space(3)))
; __device__ __forceinline__ unsigned pk2(float lo, float hi) { return f2bf(lo) | (f2bf(hi) << 16); }
;     __device__ __forceinline__ const float* x() const { return (const float*)ld(0); }
;     __device__ __forceinline__ const float* c() const { return (const float*)ld(1); }
; template <bool NT = true> __device__ __forceinline__ void cvt_store(const CvtItem& d, const f32x4 (&v)[8], LAS float* scr, int lane) {
;     const int rr = lane >> 3, c4 = (lane & 7) * 4;
; #pragma unroll
;     for (int q = 0; q < 8; ++q) { LAS float* t = scr + (8 * q + rr) * 33 + c4; t[0] = v[q].x; t[1] = v[q].y; t[2] = v[q].z; t[3] = v[q].w; }
;     asm volatile("s_waitcnt lgkmcnt(0)" ::: "memory");
;     const int c = lane & 7;
; #pragma unroll
;     for (int j = 0; j < 4; ++j) { const int n = (lane >> 3) + 8 * j; const LAS float* s = scr + (8 * c) * 33 + n;
;         u32x4 o; o.x = pk2(s[0 * 33], s[1 * 33]); o.y = pk2(s[2 * 33], s[3 * 33]); o.z = pk2(s[4 * 33], s[5 * 33]); o.w = pk2(s[6 * 33], s[7 * 33]);
;         const int ng = d.n0 + n, drow = d.row_off + (d.ilv ? ((ng >> 7) * 256 + (ng & 127)) : ng);
;         if (NT) __builtin_nontemporal_store(o, (u32x4*)(d.dst + (size_t)drow * d.K + d.k0 + 8 * c)); else *(u32x4*)(d.dst + (size_t)drow * d.K + d.k0 + 8 * c) = o; }
;     asm volatile("s_waitcnt lgkmcnt(0)" ::: "memory");
.LBB0_532:
	s_add_i32 s2, s55, 0x4000
	s_cmpk_lg_u32 s55, 0x8000
	s_cselect_b32 s57, s2, 0
	v_mfma_f32_32x32x16_bf16 v[66:81], v[194:197], v[166:169], v[66:81]
	v_exp_f32_e32 v130, v130
	v_exp_f32_e32 v131, v131
	ds_read_b64_tr_b16 v[154:155], v16 offset:50176
	ds_read_b64_tr_b16 v[156:157], v16 offset:50688
	s_add_u32 s2, s58, 0x80000
	s_addc_u32 s3, s59, 0
	s_add_i32 s60, s55, s49
	s_mov_b32 s61, m0
	s_mov_b32 m0, s60
	s_nop 0
	global_load_lds_dwordx4 v237, s[2:3] offset:0
	s_mov_b32 m0, s61
	v_mfma_f32_32x32x16_bf16 v[82:97], v[194:197], v[162:165], v[82:97]
	v_exp_f32_e32 v132, v132
	v_exp_f32_e32 v133, v133
	ds_read_b64_tr_b16 v[158:159], v16 offset:54272
	ds_read_b64_tr_b16 v[160:161], v16 offset:54784
	s_waitcnt lgkmcnt(6)
	v_mfma_f32_32x32x16_bf16 v[34:49], v[194:197], v[150:153], v[34:49]
	v_exp_f32_e32 v134, v134
	v_exp_f32_e32 v135, v135
	ds_read_b64_tr_b16 v[162:163], v16 offset:58368
	ds_read_b64_tr_b16 v[164:165], v16 offset:58880
	s_add_u32 s2, s58, 0x80080
	s_addc_u32 s3, s59, 0
	s_add_i32 s58, s55, s54
	s_mov_b32 s59, m0
	s_mov_b32 m0, s58
	s_nop 0
	global_load_lds_dwordx4 v237, s[2:3] offset:0
	s_mov_b32 m0, s59
	s_waitcnt lgkmcnt(6)
	v_mfma_f32_32x32x16_bf16 v[50:65], v[194:197], v[146:149], v[50:65]
	v_exp_f32_e32 v136, v136
	v_exp_f32_e32 v137, v137
	ds_read_b64_tr_b16 v[150:151], v16 offset:62464
	ds_read_b64_tr_b16 v[152:153], v16 offset:62976
	v_add_u32_e32 v3, s57, v236
	ds_read_b128 v[146:149], v3
	ds_read_b128 v[202:205], v3 offset:512
	s_waitcnt lgkmcnt(8)
	v_mfma_f32_32x32x16_bf16 v[66:81], v[12:15], v[154:157], v[66:81]
	v_exp_f32_e32 v138, v138
	v_exp_f32_e32 v139, v139
	ds_read_b64_tr_b16 v[166:167], v16 offset:51200
	ds_read_b64_tr_b16 v[168:169], v16 offset:51712
	s_add_u32 s2, s33, 0x40000
	s_addc_u32 s3, s53, 0
	s_add_i32 s58, s57, s46
	s_mov_b32 s59, m0
	s_mov_b32 m0, s58
	s_nop 0
	global_load_lds_dwordx4 v235, s[2:3] offset:0
	s_mov_b32 m0, s59
	s_waitcnt lgkmcnt(8)
	v_mfma_f32_32x32x16_bf16 v[82:97], v[12:15], v[158:161], v[82:97]
	v_exp_f32_e32 v140, v140
	v_exp_f32_e32 v141, v141
	ds_read_b64_tr_b16 v[154:155], v16 offset:55296
	ds_read_b64_tr_b16 v[156:157], v16 offset:55808
	ds_read_b128 v[206:209], v3 offset:2048
	ds_read_b128 v[190:193], v3 offset:2560
	s_waitcnt lgkmcnt(10)
	v_mfma_f32_32x32x16_bf16 v[34:49], v[12:15], v[162:165], v[34:49]
	v_exp_f32_e32 v142, v142
	v_exp_f32_e32 v143, v143
	ds_read_b64_tr_b16 v[158:159], v16 offset:59392
	ds_read_b64_tr_b16 v[160:161], v16 offset:59904
	s_add_u32 s2, s33, 0x40080
	s_addc_u32 s3, s53, 0
	s_add_i32 s58, s57, s45
	s_mov_b32 s59, m0
	s_mov_b32 m0, s58
	s_nop 0
	global_load_lds_dwordx4 v235, s[2:3] offset:0
	s_mov_b32 m0, s59
	s_waitcnt lgkmcnt(10)
	v_mfma_f32_32x32x16_bf16 v[50:65], v[12:15], v[150:153], v[50:65]
	v_exp_f32_e32 v144, v144
	v_exp_f32_e32 v145, v145
	ds_read_b64_tr_b16 v[162:163], v16 offset:63488
	ds_read_b64_tr_b16 v[164:165], v16 offset:64000
	ds_read_b128 v[198:201], v3 offset:4096
	ds_read_b128 v[186:189], v3 offset:4608
	s_waitcnt lgkmcnt(10)
	v_mfma_f32_32x32x16_bf16 v[66:81], v[8:11], v[166:169], v[66:81]
	v_exp_f32_e32 v114, v114
	v_exp_f32_e32 v115, v115
	ds_read_b64_tr_b16 v[150:151], v16 offset:52224
	ds_read_b64_tr_b16 v[152:153], v16 offset:52736
	s_waitcnt lgkmcnt(10)
	v_mfma_f32_32x32x16_bf16 v[82:97], v[8:11], v[154:157], v[82:97]
	v_exp_f32_e32 v116, v116
	v_exp_f32_e32 v117, v117
	ds_read_b64_tr_b16 v[166:167], v16 offset:56320
	ds_read_b64_tr_b16 v[168:169], v16 offset:56832
	ds_read_b128 v[182:185], v3 offset:6144
	ds_read_b128 v[178:181], v3 offset:6656
	s_waitcnt lgkmcnt(10)
	v_mfma_f32_32x32x16_bf16 v[34:49], v[8:11], v[158:161], v[34:49]
	v_exp_f32_e32 v118, v118
	v_exp_f32_e32 v119, v119
	ds_read_b64_tr_b16 v[154:155], v16 offset:60416
	ds_read_b64_tr_b16 v[156:157], v16 offset:60928
	s_waitcnt lgkmcnt(10)
	v_mfma_f32_32x32x16_bf16 v[50:65], v[8:11], v[162:165], v[50:65]
	v_exp_f32_e32 v120, v120
	v_exp_f32_e32 v121, v121
	ds_read_b64_tr_b16 v[158:159], v16 offset:64512
	ds_read_b64_tr_b16 v[160:161], v16 offset:65024
	s_waitcnt lgkmcnt(8)
	v_mfma_f32_32x32x16_bf16 v[66:81], v[4:7], v[150:153], v[66:81]
	v_exp_f32_e32 v122, v122
	v_exp_f32_e32 v123, v123
	s_waitcnt lgkmcnt(6)
	v_mfma_f32_32x32x16_bf16 v[82:97], v[4:7], v[166:169], v[82:97]
	v_exp_f32_e32 v124, v124
	v_exp_f32_e32 v125, v125
	s_waitcnt lgkmcnt(2)
	v_mfma_f32_32x32x16_bf16 v[34:49], v[4:7], v[154:157], v[34:49]
	v_exp_f32_e32 v126, v126
	v_exp_f32_e32 v127, v127
	s_waitcnt lgkmcnt(0)
	v_mfma_f32_32x32x16_bf16 v[50:65], v[4:7], v[158:161], v[50:65]
	v_exp_f32_e32 v128, v128
	v_exp_f32_e32 v129, v129
	s_add_i32 s2, s56, 2
	s_cmp_gt_i32 s2, s90
	s_cbranch_scc1 .Lcs_done_h1
	s_waitcnt vmcnt(6)
	v_cvt_pk_bf16_f32 v245, v18, v19
	v_cvt_pk_bf16_f32 v244, v20, v21
	s_cmp_lt_u32 s2, 7
	s_cbranch_scc1 .Lcs_dumS_h1
	s_and_b32 s61, s2, 7
	s_cmp_eq_u32 s61, 7
	s_cbranch_scc1 .Lcs_adopt_h1

; #define LAS __attribute__((address_space(3)))
; __device__ __forceinline__ unsigned pk2(float lo, float hi) { return f2bf(lo) | (f2bf(hi) << 16); }
;     __device__ __forceinline__ const float* x() const { return (const float*)ld(0); }
;     __device__ __forceinline__ const float* c() const { return (const float*)ld(1); }
; template <bool NT = true> __device__ __forceinline__ void cvt_store(const CvtItem& d, const f32x4 (&v)[8], LAS float* scr, int lane) {
;     const int rr = lane >> 3, c4 = (lane & 7) * 4;
; #pragma unroll
;     for (int q = 0; q < 8; ++q) { LAS float* t = scr + (8 * q + rr) * 33 + c4; t[0] = v[q].x; t[1] = v[q].y; t[2] = v[q].z; t[3] = v[q].w; }
;     asm volatile("s_waitcnt lgkmcnt(0)" ::: "memory");
;     const int c = lane & 7;
; #pragma unroll
;     for (int j = 0; j < 4; ++j) { const int n = (lane >> 3) + 8 * j; const LAS float* s = scr + (8 * c) * 33 + n;
;         u32x4 o; o.x = pk2(s[0 * 33], s[1 * 33]); o.y = pk2(s[2 * 33], s[3 * 33]); o.z = pk2(s[4 * 33], s[5 * 33]); o.w = pk2(s[6 * 33], s[7 * 33]);
;         const int ng = d.n0 + n, drow = d.row_off + (d.ilv ? ((ng >> 7) * 256 + (ng & 127)) : ng);
;         if (NT) __builtin_nontemporal_store(o, (u32x4*)(d.dst + (size_t)drow * d.K + d.k0 + 8 * c)); else *(u32x4*)(d.dst + (size_t)drow * d.K + d.k0 + 8 * c) = o; }
;     asm volatile("s_waitcnt lgkmcnt(0)" ::: "memory");
.Lcs_noL_h1:
	s_waitcnt lgkmcnt(0)
	s_cmp_gt_i32 s2, s90
	s_cbranch_scc1 .Lcs_noW_h1
	ds_write_b16 v29, v245
	ds_write_b16_d16_hi v29, v245 offset:64
	ds_write_b16 v29, v244 offset:128
	ds_write_b16_d16_hi v29, v244 offset:192
	s_bitcmp1_b32 s2, 1
	s_cselect_b32 s3, 16, -48
	v_add_u32_e32 v29, s3, v29
